# causal-mask attention body: second half-step also swapped for waves 4-7 via an out-of-line QK^T copy that reads K into registers dead after finishSM
# baseline (speedup 1.0000x reference)
.LBB0_1266:
	v_cndmask_b32_e64 v176, v146, v200, s[2:3]
	s_waitcnt lgkmcnt(0)
	s_barrier
	v_mul_f32_e32 v150, 0xbe0293ee, v176
	v_fmamk_f32 v66, v66, 0x3e0293ee, v150
	v_fmamk_f32 v67, v67, 0x3e0293ee, v150
	v_fmamk_f32 v68, v68, 0x3e0293ee, v150
	v_fmamk_f32 v69, v69, 0x3e0293ee, v150
	v_fmamk_f32 v70, v70, 0x3e0293ee, v150
	v_fmamk_f32 v71, v71, 0x3e0293ee, v150
	v_fmamk_f32 v72, v72, 0x3e0293ee, v150
	v_fmamk_f32 v73, v73, 0x3e0293ee, v150
	v_fmamk_f32 v74, v74, 0x3e0293ee, v150
	v_fmamk_f32 v75, v75, 0x3e0293ee, v150
	v_fmamk_f32 v76, v76, 0x3e0293ee, v150
	v_fmamk_f32 v77, v77, 0x3e0293ee, v150
	v_fmamk_f32 v78, v78, 0x3e0293ee, v150
	v_fmamk_f32 v79, v79, 0x3e0293ee, v150
	v_fmamk_f32 v80, v80, 0x3e0293ee, v150
	v_fmamk_f32 v81, v81, 0x3e0293ee, v150
	v_fmamk_f32 v151, v82, 0x3e0293ee, v150
	v_fmamk_f32 v152, v83, 0x3e0293ee, v150
	v_fmamk_f32 v153, v84, 0x3e0293ee, v150
	v_fmamk_f32 v154, v85, 0x3e0293ee, v150
	v_fmamk_f32 v155, v86, 0x3e0293ee, v150
	v_fmamk_f32 v156, v87, 0x3e0293ee, v150
	v_fmamk_f32 v157, v88, 0x3e0293ee, v150
	v_fmamk_f32 v158, v89, 0x3e0293ee, v150
	v_fmamk_f32 v159, v90, 0x3e0293ee, v150
	v_fmamk_f32 v160, v91, 0x3e0293ee, v150
	v_fmamk_f32 v161, v92, 0x3e0293ee, v150
	v_fmamk_f32 v178, v93, 0x3e0293ee, v150
	v_fmamk_f32 v179, v94, 0x3e0293ee, v150
	v_fmamk_f32 v200, v95, 0x3e0293ee, v150
	v_fmamk_f32 v206, v96, 0x3e0293ee, v150
	v_fmac_f32_e32 v150, 0x3e0293ee, v97
	v_exp_f32_e32 v208, v66
	v_exp_f32_e32 v209, v67
	v_exp_f32_e32 v210, v68
	v_exp_f32_e32 v211, v69
	v_exp_f32_e32 v212, v70
	v_exp_f32_e32 v213, v71
	v_exp_f32_e32 v214, v72
	v_exp_f32_e32 v215, v73
	v_exp_f32_e32 v216, v74
	v_exp_f32_e32 v217, v75
	v_exp_f32_e32 v218, v76
	v_exp_f32_e32 v219, v77
	v_exp_f32_e32 v220, v78
	v_exp_f32_e32 v221, v79
	v_exp_f32_e32 v222, v80
	v_exp_f32_e32 v223, v81
	s_add_i32 s2, s85, 1
	v_readlane_b32 vcc_lo, v255, 63
	s_bitcmp1_b32 vcc_lo, 0
	s_cbranch_scc1 .Lswq_B
.Lswq_A:
	v_cvt_f32_i32_e32 v66, v199
	s_lshr_b32 s2, s2, 8
	v_lshrrev_b32_sdwa v67, s2, v192 dst_sel:DWORD dst_unused:UNUSED_PAD src0_sel:DWORD src1_sel:WORD_0
	v_and_b32_e32 v67, 1, v67
	v_mul_f32_e64 v66, -v162, v66
	v_cmp_eq_u32_e32 vcc, 1, v67
	s_mov_b32 s2, 0x41900000
	s_mov_b32 s3, 0x41980000
	v_cndmask_b32_e32 v82, v243, v66, vcc
	v_pk_fma_f32 v[76:77], v[170:171], s[2:3], v[82:83] op_sel_hi:[1,1,0]
	s_mov_b32 s2, 0x41c00000
	s_mov_b32 s3, 0x41c80000
	v_pk_fma_f32 v[78:79], v[170:171], s[2:3], v[82:83] op_sel_hi:[1,1,0]
	s_mov_b32 s2, 0x41d00000
	s_mov_b32 s3, 0x41d80000
	v_pk_fma_f32 v[80:81], v[170:171], s[2:3], v[82:83] op_sel_hi:[1,1,0]
	s_mov_b32 s2, 0x42000000
	v_mov_b32_e32 v163, v162
	s_mov_b32 s3, 0x42040000
	v_fma_f32 v66, 0, v162, v82
	v_add_f32_e32 v67, v162, v82
	v_pk_fma_f32 v[68:69], v[170:171], s[60:61], v[82:83] op_sel_hi:[1,1,0]
	v_pk_fma_f32 v[70:71], v[170:171], s[74:75], v[82:83] op_sel_hi:[1,1,0]
	v_pk_fma_f32 v[72:73], v[170:171], s[62:63], v[82:83] op_sel_hi:[1,1,0]
	v_pk_fma_f32 v[74:75], v[170:171], s[58:59], v[82:83] op_sel_hi:[1,1,0]
	v_pk_fma_f32 v[96:97], v[162:163], s[68:69], v[82:83] op_sel_hi:[1,1,0]
	v_pk_fma_f32 v[94:95], v[162:163], s[96:97], v[82:83] op_sel_hi:[1,1,0]
	v_pk_fma_f32 v[92:93], v[162:163], s[94:95], v[82:83] op_sel_hi:[1,1,0]
	v_pk_fma_f32 v[90:91], v[162:163], s[92:93], v[82:83] op_sel_hi:[1,1,0]
	v_pk_fma_f32 v[88:89], v[162:163], s[90:91], v[82:83] op_sel_hi:[1,1,0]
	v_pk_fma_f32 v[86:87], v[162:163], s[88:89], v[82:83] op_sel_hi:[1,1,0]
	v_pk_fma_f32 v[84:85], v[162:163], s[86:87], v[82:83] op_sel_hi:[1,1,0]
	v_pk_fma_f32 v[82:83], v[168:169], s[2:3], v[82:83] op_sel_hi:[1,1,0]
	s_setprio 1
	ds_read_b128 v[146:149], v195 offset:32768
	ds_read_b128 v[224:227], v195 offset:40960
	s_waitcnt lgkmcnt(1)
	v_mfma_f32_32x32x16_bf16 v[66:81], v[146:149], v[126:129], v[66:81]
	ds_read_b128 v[146:149], v196 offset:32768
	s_waitcnt lgkmcnt(1)
	v_mfma_f32_32x32x16_bf16 v[82:97], v[224:227], v[126:129], v[82:97]
	ds_read_b128 v[224:227], v196 offset:40960
	s_waitcnt lgkmcnt(1)
	v_mfma_f32_32x32x16_bf16 v[66:81], v[146:149], v[122:125], v[66:81]
	ds_read_b128 v[146:149], v197 offset:32768
	s_waitcnt lgkmcnt(1)
	v_mfma_f32_32x32x16_bf16 v[82:97], v[224:227], v[122:125], v[82:97]
	ds_read_b128 v[224:227], v197 offset:40960
	s_waitcnt lgkmcnt(1)
	v_mfma_f32_32x32x16_bf16 v[66:81], v[146:149], v[118:121], v[66:81]
	ds_read_b128 v[146:149], v198 offset:32768
	s_waitcnt lgkmcnt(1)
	v_mfma_f32_32x32x16_bf16 v[82:97], v[224:227], v[118:121], v[82:97]
	ds_read_b128 v[224:227], v198 offset:40960
	s_waitcnt lgkmcnt(1)
	v_mfma_f32_32x32x16_bf16 v[66:81], v[146:149], v[114:117], v[66:81]
	ds_read_b128 v[146:149], v195 offset:32896
	s_waitcnt lgkmcnt(1)
	v_mfma_f32_32x32x16_bf16 v[82:97], v[224:227], v[114:117], v[82:97]
	ds_read_b128 v[224:227], v195 offset:41088
	s_waitcnt lgkmcnt(1)
	v_mfma_f32_32x32x16_bf16 v[66:81], v[146:149], v[110:113], v[66:81]
	ds_read_b128 v[146:149], v196 offset:32896
	s_waitcnt lgkmcnt(1)
	v_mfma_f32_32x32x16_bf16 v[82:97], v[224:227], v[110:113], v[82:97]
	ds_read_b128 v[224:227], v196 offset:41088
	s_waitcnt lgkmcnt(1)
	v_mfma_f32_32x32x16_bf16 v[66:81], v[146:149], v[106:109], v[66:81]
	ds_read_b128 v[146:149], v197 offset:32896
	s_waitcnt lgkmcnt(1)
	v_mfma_f32_32x32x16_bf16 v[82:97], v[224:227], v[106:109], v[82:97]
	ds_read_b128 v[224:227], v197 offset:41088
	s_waitcnt lgkmcnt(1)
	v_mfma_f32_32x32x16_bf16 v[66:81], v[146:149], v[102:105], v[66:81]
	ds_read_b128 v[146:149], v198 offset:32896
	s_waitcnt lgkmcnt(1)
	v_mfma_f32_32x32x16_bf16 v[82:97], v[224:227], v[102:105], v[82:97]
	ds_read_b128 v[224:227], v198 offset:41088
	s_waitcnt lgkmcnt(1)
	v_mfma_f32_32x32x16_bf16 v[66:81], v[146:149], v[98:101], v[66:81]
	s_waitcnt lgkmcnt(0)
	v_mfma_f32_32x32x16_bf16 v[82:97], v[224:227], v[98:101], v[82:97]
	s_setprio 0
.Lswq_B:
	v_add_f32_e32 v146, 0, v208
	v_add_f32_e32 v146, v209, v146
	v_add_f32_e32 v146, v210, v146
	v_add_f32_e32 v146, v211, v146
	v_add_f32_e32 v146, v212, v146
	v_add_f32_e32 v146, v213, v146
	v_add_f32_e32 v146, v214, v146
	v_add_f32_e32 v146, v215, v146
	v_add_f32_e32 v146, v216, v146
	v_add_f32_e32 v146, v217, v146
	v_add_f32_e32 v146, v218, v146
	v_add_f32_e32 v146, v219, v146
	v_exp_f32_e32 v225, v151
	v_add_f32_e32 v146, v220, v146
	v_exp_f32_e32 v226, v152
	v_add_f32_e32 v146, v221, v146
	v_exp_f32_e32 v227, v153
	v_add_f32_e32 v146, v222, v146
	v_exp_f32_e32 v228, v154
	v_add_f32_e32 v146, v223, v146
	v_exp_f32_e32 v229, v155
	v_add_f32_e32 v146, v225, v146
	v_exp_f32_e32 v156, v156
	v_add_f32_e32 v146, v226, v146
	v_exp_f32_e32 v157, v157
	v_add_f32_e32 v146, v227, v146
	v_exp_f32_e32 v158, v158
	v_add_f32_e32 v146, v228, v146
	v_exp_f32_e32 v159, v159
	v_add_f32_e32 v146, v229, v146
	v_exp_f32_e32 v160, v160
	v_add_f32_e32 v146, v156, v146
	v_exp_f32_e32 v161, v161
	v_add_f32_e32 v146, v157, v146
	v_exp_f32_e32 v178, v178
	v_add_f32_e32 v146, v158, v146
	v_exp_f32_e32 v179, v179
	v_add_f32_e32 v146, v159, v146
	v_exp_f32_e32 v200, v200
	v_add_f32_e32 v146, v160, v146
	v_exp_f32_e32 v206, v206
	v_add_f32_e32 v146, v161, v146
	v_exp_f32_e32 v230, v150
	v_add_f32_e32 v146, v178, v146
	v_add_f32_e32 v146, v179, v146
	v_add_f32_e32 v146, v200, v146
	v_add_f32_e32 v146, v206, v146
	v_add_f32_e32 v163, v230, v146
	v_mov_b32_e32 v224, v163
	v_cvt_pk_bf16_f32 v146, v208, v209
	v_cvt_pk_bf16_f32 v147, v210, v211
	v_cvt_pk_bf16_f32 v148, v212, v213
	v_cvt_pk_bf16_f32 v149, v214, v215
	v_cvt_pk_bf16_f32 v150, v216, v217
	v_cvt_pk_bf16_f32 v151, v218, v219
	v_cvt_pk_bf16_f32 v152, v220, v221
	v_cvt_pk_bf16_f32 v153, v222, v223
	v_cvt_pk_bf16_f32 v154, v225, v226
	v_cvt_pk_bf16_f32 v155, v227, v228
	v_cvt_pk_bf16_f32 v156, v229, v156
	v_cvt_pk_bf16_f32 v157, v157, v158
	v_cvt_pk_bf16_f32 v158, v159, v160
	v_cvt_pk_bf16_f32 v159, v161, v178
	v_cvt_pk_bf16_f32 v160, v179, v200
	v_cvt_pk_bf16_f32 v161, v206, v230
	s_nop 1
	v_permlane32_swap_b32_e32 v163, v224
	v_permlane32_swap_b32_e32 v146, v148
	v_permlane32_swap_b32_e32 v147, v149
	v_permlane32_swap_b32_e32 v150, v152
	v_permlane32_swap_b32_e32 v151, v153
	v_permlane32_swap_b32_e32 v154, v156
	v_permlane32_swap_b32_e32 v155, v157
	v_permlane32_swap_b32_e32 v158, v160
	v_permlane32_swap_b32_e32 v159, v161
	v_readlane_b32 vcc_lo, v255, 63
	s_bitcmp1_b32 vcc_lo, 0
	s_cbranch_scc1 .Lswq_A2
.Lswq_done:
	s_add_i32 s2, s84, 1
	s_cmp_lt_u32 s2, s83
	s_cselect_b64 s[76:77], -1, 0
	s_cmp_ge_u32 s2, s83
	s_cbranch_scc1 .LBB0_1268
	v_add_u32_e32 v138, 0x41, v177
	v_add_u32_e32 v140, 0x61, v177
	v_mad_i64_i32 v[130:131], s[2:3], v138, s71, v[172:173]
	v_mad_i64_i32 v[134:135], s[2:3], v140, s71, v[172:173]
	v_mad_i64_i32 v[138:139], s[2:3], v138, s71, v[174:175]
	v_mad_i64_i32 v[142:143], s[2:3], v140, s71, v[174:175]
	global_load_dwordx4 v[130:133], v[130:131], off
	s_nop 0
	global_load_dwordx4 v[134:137], v[134:135], off
	s_nop 0
	global_load_dwordx4 v[138:141], v[138:139], off
	s_nop 0
	global_load_dwordx4 v[142:145], v[142:143], off

.Lswq_A2:
	v_cvt_f32_i32_e32 v66, v199
	s_lshr_b32 s2, s2, 8
	v_lshrrev_b32_sdwa v67, s2, v192 dst_sel:DWORD dst_unused:UNUSED_PAD src0_sel:DWORD src1_sel:WORD_0
	v_and_b32_e32 v67, 1, v67
	v_mul_f32_e64 v66, -v162, v66
	v_cmp_eq_u32_e32 vcc, 1, v67
	s_mov_b32 s2, 0x41900000
	s_mov_b32 s3, 0x41980000
	v_cndmask_b32_e32 v82, v243, v66, vcc
	v_pk_fma_f32 v[76:77], v[170:171], s[2:3], v[82:83] op_sel_hi:[1,1,0]
	s_mov_b32 s2, 0x41c00000
	s_mov_b32 s3, 0x41c80000
	v_pk_fma_f32 v[78:79], v[170:171], s[2:3], v[82:83] op_sel_hi:[1,1,0]
	s_mov_b32 s2, 0x41d00000
	s_mov_b32 s3, 0x41d80000
	v_pk_fma_f32 v[80:81], v[170:171], s[2:3], v[82:83] op_sel_hi:[1,1,0]
	s_mov_b32 s2, 0x42000000
	v_mov_b32_e32 v208, v162
	v_mov_b32_e32 v209, v162
	s_mov_b32 s3, 0x42040000
	v_fma_f32 v66, 0, v162, v82
	v_add_f32_e32 v67, v162, v82
	v_pk_fma_f32 v[68:69], v[170:171], s[60:61], v[82:83] op_sel_hi:[1,1,0]
	v_pk_fma_f32 v[70:71], v[170:171], s[74:75], v[82:83] op_sel_hi:[1,1,0]
	v_pk_fma_f32 v[72:73], v[170:171], s[62:63], v[82:83] op_sel_hi:[1,1,0]
	v_pk_fma_f32 v[74:75], v[170:171], s[58:59], v[82:83] op_sel_hi:[1,1,0]
	v_pk_fma_f32 v[96:97], v[208:209], s[68:69], v[82:83] op_sel_hi:[1,1,0]
	v_pk_fma_f32 v[94:95], v[208:209], s[96:97], v[82:83] op_sel_hi:[1,1,0]
	v_pk_fma_f32 v[92:93], v[208:209], s[94:95], v[82:83] op_sel_hi:[1,1,0]
	v_pk_fma_f32 v[90:91], v[208:209], s[92:93], v[82:83] op_sel_hi:[1,1,0]
	v_pk_fma_f32 v[88:89], v[208:209], s[90:91], v[82:83] op_sel_hi:[1,1,0]
	v_pk_fma_f32 v[86:87], v[208:209], s[88:89], v[82:83] op_sel_hi:[1,1,0]
	v_pk_fma_f32 v[84:85], v[208:209], s[86:87], v[82:83] op_sel_hi:[1,1,0]
	v_pk_fma_f32 v[82:83], v[168:169], s[2:3], v[82:83] op_sel_hi:[1,1,0]
	s_setprio 1
	ds_read_b128 v[212:215], v195 offset:32768
	ds_read_b128 v[216:219], v195 offset:40960
	ds_read_b128 v[220:223], v196 offset:32768
	ds_read_b128 v[226:229], v196 offset:40960
	s_waitcnt lgkmcnt(3)
	v_mfma_f32_32x32x16_bf16 v[66:81], v[212:215], v[126:129], v[66:81]
	ds_read_b128 v[212:215], v197 offset:32768
	s_waitcnt lgkmcnt(3)
	v_mfma_f32_32x32x16_bf16 v[82:97], v[216:219], v[126:129], v[82:97]
	ds_read_b128 v[216:219], v197 offset:40960
	s_waitcnt lgkmcnt(3)
	v_mfma_f32_32x32x16_bf16 v[66:81], v[220:223], v[122:125], v[66:81]
	ds_read_b128 v[220:223], v198 offset:32768
	s_waitcnt lgkmcnt(3)
	v_mfma_f32_32x32x16_bf16 v[82:97], v[226:229], v[122:125], v[82:97]
	ds_read_b128 v[226:229], v198 offset:40960
	s_waitcnt lgkmcnt(3)
	v_mfma_f32_32x32x16_bf16 v[66:81], v[212:215], v[118:121], v[66:81]
	ds_read_b128 v[212:215], v195 offset:32896
	s_waitcnt lgkmcnt(3)
	v_mfma_f32_32x32x16_bf16 v[82:97], v[216:219], v[118:121], v[82:97]
	ds_read_b128 v[216:219], v195 offset:41088
	s_waitcnt lgkmcnt(3)
	v_mfma_f32_32x32x16_bf16 v[66:81], v[220:223], v[114:117], v[66:81]
	ds_read_b128 v[220:223], v196 offset:32896
	s_waitcnt lgkmcnt(3)
	v_mfma_f32_32x32x16_bf16 v[82:97], v[226:229], v[114:117], v[82:97]
	ds_read_b128 v[226:229], v196 offset:41088
	s_waitcnt lgkmcnt(3)
	v_mfma_f32_32x32x16_bf16 v[66:81], v[212:215], v[110:113], v[66:81]
	ds_read_b128 v[212:215], v197 offset:32896
	s_waitcnt lgkmcnt(3)
	v_mfma_f32_32x32x16_bf16 v[82:97], v[216:219], v[110:113], v[82:97]
	ds_read_b128 v[216:219], v197 offset:41088
	s_waitcnt lgkmcnt(3)
	v_mfma_f32_32x32x16_bf16 v[66:81], v[220:223], v[106:109], v[66:81]
	ds_read_b128 v[220:223], v198 offset:32896
	s_waitcnt lgkmcnt(3)
	v_mfma_f32_32x32x16_bf16 v[82:97], v[226:229], v[106:109], v[82:97]
	ds_read_b128 v[226:229], v198 offset:41088
	s_waitcnt lgkmcnt(3)
	v_mfma_f32_32x32x16_bf16 v[66:81], v[212:215], v[102:105], v[66:81]
	s_waitcnt lgkmcnt(2)
	v_mfma_f32_32x32x16_bf16 v[82:97], v[216:219], v[102:105], v[82:97]
	s_waitcnt lgkmcnt(1)
	v_mfma_f32_32x32x16_bf16 v[66:81], v[220:223], v[98:101], v[66:81]
	s_waitcnt lgkmcnt(0)
	v_mfma_f32_32x32x16_bf16 v[82:97], v[226:229], v[98:101], v[82:97]
	s_setprio 0
	s_branch .Lswq_done
